# k5_pk_epi
# baseline (speedup 1.0000x reference)
.Lg0_cloop:
	s_mul_i32 s8, s3, 0x7000
	s_barrier
	v_add_u32_e32 v103, s8, v100
	v_add_u32_e32 v101, s8, v99
	ds_read_b128 v[146:149], v103 offset:12288
	ds_read_b128 v[150:153], v103 offset:13312
	ds_read_b128 v[154:157], v103 offset:14336
	ds_read_b128 v[158:161], v103 offset:15360
	s_waitcnt lgkmcnt(9)
	v_mfma_f32_16x16x32_f16 v[94:97], v[122:125], v[104:107], v[94:97]
	s_add_i32 s8, s3, 1
	s_cmp_lg_u32 s3, 4
	s_cselect_b32 s3, s8, 0
	v_mfma_f32_16x16x32_f16 v[70:73], v[122:125], v[108:111], v[70:73]
	v_mfma_f32_16x16x32_f16 v[46:49], v[122:125], v[112:115], v[46:49]
	v_mfma_f32_16x16x32_f16 v[22:25], v[122:125], v[116:119], v[22:25]
	ds_read_b128 v[122:125], v101
	s_waitcnt lgkmcnt(9)
	v_mfma_f32_16x16x32_f16 v[90:93], v[126:129], v[104:107], v[90:93]
	v_mfma_f32_16x16x32_f16 v[66:69], v[126:129], v[108:111], v[66:69]
	v_mfma_f32_16x16x32_f16 v[42:45], v[126:129], v[112:115], v[42:45]
	v_mfma_f32_16x16x32_f16 v[18:21], v[126:129], v[116:119], v[18:21]
	ds_read_b128 v[126:129], v101 offset:1024
	s_waitcnt lgkmcnt(9)
	v_mfma_f32_16x16x32_f16 v[86:89], v[130:133], v[104:107], v[86:89]
	v_mfma_f32_16x16x32_f16 v[54:57], v[130:133], v[108:111], v[54:57]
	v_mfma_f32_16x16x32_f16 v[26:29], v[130:133], v[112:115], v[26:29]
	v_mfma_f32_16x16x32_f16 v[6:9], v[130:133], v[116:119], v[6:9]
	ds_read_b128 v[130:133], v101 offset:2048
	s_waitcnt lgkmcnt(9)
	v_mfma_f32_16x16x32_f16 v[74:77], v[134:137], v[104:107], v[74:77]
	v_mfma_f32_16x16x32_f16 v[50:53], v[134:137], v[108:111], v[50:53]
	v_mfma_f32_16x16x32_f16 v[38:41], v[134:137], v[112:115], v[38:41]
	v_mfma_f32_16x16x32_f16 v[14:17], v[134:137], v[116:119], v[14:17]
	ds_read_b128 v[134:137], v101 offset:3072
	s_waitcnt lgkmcnt(9)
	v_mfma_f32_16x16x32_f16 v[82:85], v[138:141], v[104:107], v[82:85]
	v_mfma_f32_16x16x32_f16 v[58:61], v[138:141], v[108:111], v[58:61]
	v_mfma_f32_16x16x32_f16 v[30:33], v[138:141], v[112:115], v[30:33]
	v_mfma_f32_16x16x32_f16 v[10:13], v[138:141], v[116:119], v[10:13]
	ds_read_b128 v[138:141], v101 offset:4096
	s_waitcnt lgkmcnt(9)
	v_mfma_f32_16x16x32_f16 v[78:81], v[142:145], v[104:107], v[78:81]
	v_mfma_f32_16x16x32_f16 v[62:65], v[142:145], v[108:111], v[62:65]
	v_mfma_f32_16x16x32_f16 v[34:37], v[142:145], v[112:115], v[34:37]
	v_mfma_f32_16x16x32_f16 v[2:5], v[142:145], v[116:119], v[2:5]
	ds_read_b128 v[142:145], v101 offset:5120
	s_mul_i32 s8, s3, 0x7000
	s_barrier
	v_add_u32_e32 v103, s8, v100
	v_add_u32_e32 v101, s8, v99
	ds_read_b128 v[104:107], v103 offset:12288
	ds_read_b128 v[108:111], v103 offset:13312
	ds_read_b128 v[112:115], v103 offset:14336
	ds_read_b128 v[116:119], v103 offset:15360
	s_waitcnt lgkmcnt(9)
	v_mfma_f32_16x16x32_f16 v[94:97], v[122:125], v[146:149], v[94:97]
	s_add_i32 s8, s3, 1
	s_cmp_lg_u32 s3, 4
	s_cselect_b32 s3, s8, 0
	v_mfma_f32_16x16x32_f16 v[70:73], v[122:125], v[150:153], v[70:73]
	v_mfma_f32_16x16x32_f16 v[46:49], v[122:125], v[154:157], v[46:49]
	v_mfma_f32_16x16x32_f16 v[22:25], v[122:125], v[158:161], v[22:25]
	ds_read_b128 v[122:125], v101
	s_waitcnt lgkmcnt(9)
	v_mfma_f32_16x16x32_f16 v[90:93], v[126:129], v[146:149], v[90:93]
	v_mfma_f32_16x16x32_f16 v[66:69], v[126:129], v[150:153], v[66:69]
	v_mfma_f32_16x16x32_f16 v[42:45], v[126:129], v[154:157], v[42:45]
	v_mfma_f32_16x16x32_f16 v[18:21], v[126:129], v[158:161], v[18:21]
	ds_read_b128 v[126:129], v101 offset:1024
	s_waitcnt lgkmcnt(9)
	v_mfma_f32_16x16x32_f16 v[86:89], v[130:133], v[146:149], v[86:89]
	v_mfma_f32_16x16x32_f16 v[54:57], v[130:133], v[150:153], v[54:57]
	v_mfma_f32_16x16x32_f16 v[26:29], v[130:133], v[154:157], v[26:29]
	v_mfma_f32_16x16x32_f16 v[6:9], v[130:133], v[158:161], v[6:9]
	ds_read_b128 v[130:133], v101 offset:2048
	s_waitcnt lgkmcnt(9)
	v_mfma_f32_16x16x32_f16 v[74:77], v[134:137], v[146:149], v[74:77]
	v_mfma_f32_16x16x32_f16 v[50:53], v[134:137], v[150:153], v[50:53]
	v_mfma_f32_16x16x32_f16 v[38:41], v[134:137], v[154:157], v[38:41]
	v_mfma_f32_16x16x32_f16 v[14:17], v[134:137], v[158:161], v[14:17]
	ds_read_b128 v[134:137], v101 offset:3072
	s_waitcnt lgkmcnt(9)
	v_mfma_f32_16x16x32_f16 v[82:85], v[138:141], v[146:149], v[82:85]
	v_mfma_f32_16x16x32_f16 v[58:61], v[138:141], v[150:153], v[58:61]
	v_mfma_f32_16x16x32_f16 v[30:33], v[138:141], v[154:157], v[30:33]
	v_mfma_f32_16x16x32_f16 v[10:13], v[138:141], v[158:161], v[10:13]
	ds_read_b128 v[138:141], v101 offset:4096
	s_waitcnt lgkmcnt(9)
	v_mfma_f32_16x16x32_f16 v[78:81], v[142:145], v[146:149], v[78:81]
	v_mfma_f32_16x16x32_f16 v[62:65], v[142:145], v[150:153], v[62:65]
	v_mfma_f32_16x16x32_f16 v[34:37], v[142:145], v[154:157], v[34:37]
	v_mfma_f32_16x16x32_f16 v[2:5], v[142:145], v[158:161], v[2:5]
	ds_read_b128 v[142:145], v101 offset:5120
	s_add_i32 s7, s7, -1
	s_cmp_eq_u32 s7, 0
	s_cbranch_scc0 .Lg0_cloop
	s_waitcnt lgkmcnt(0)
	s_barrier
	s_mul_i32 s24, s22, 0x3400
	s_lshl_b32 s28, s2, 6
	s_add_i32 s29, s20, s28
	s_and_b32 s30, s29, 0x7ff
	v_add_u32_e32 v98, s30, v102
	v_lshlrev_b32_e32 v98, 8, v98
	v_lshl_add_u32 v98, v120, 4, v98
	v_add_u32_e32 v99, 0x1000, v98
	v_add_u32_e32 v100, 0x2000, v98
	v_add_u32_e32 v101, 0x3000, v98
	v_mul_u32_u24_e32 v103, 0xd0, v102
	v_lshl_add_u32 v103, v120, 3, v103
	v_add_u32_e32 v103, s24, v103
	v_lshrrev_b32_e32 v0, 2, v1
	v_and_b32_e32 v1, 3, v1
	v_mul_u32_u24_e32 v102, 0xd0, v0
	v_lshl_add_u32 v102, v1, 4, v102
	v_add_u32_e32 v102, s24, v102
	v_lshlrev_b32_e32 v0, 11, v0
	v_lshl_add_u32 v0, v1, 4, v0
	s_lshl_b32 s31, s5, 7
	s_add_i32 s35, s31, 0
	s_and_b32 s35, s35, 0xff
	s_add_u32 s36, s12, s35
	s_addc_u32 s37, s13, 0
	s_add_i32 s35, s31, 64
	s_and_b32 s35, s35, 0xff
	s_add_u32 s38, s12, s35
	s_addc_u32 s39, s13, 0
	s_add_i32 s35, s31, 128
	s_and_b32 s35, s35, 0xff
	s_add_u32 s40, s12, s35
	s_addc_u32 s41, s13, 0
	s_add_i32 s35, s31, 192
	s_and_b32 s35, s35, 0xff
	s_add_u32 s42, s12, s35
	s_addc_u32 s43, s13, 0
	global_load_dwordx4 v[104:107], v98, s[36:37]
	global_load_dwordx4 v[108:111], v98, s[38:39]
	global_load_dwordx4 v[112:115], v98, s[40:41]
	global_load_dwordx4 v[116:119], v98, s[42:43]
	global_load_dwordx4 v[120:123], v99, s[36:37]
	global_load_dwordx4 v[124:127], v99, s[38:39]
	global_load_dwordx4 v[128:131], v99, s[40:41]
	global_load_dwordx4 v[132:135], v99, s[42:43]
	global_load_dwordx4 v[136:139], v100, s[36:37]
	global_load_dwordx4 v[140:143], v100, s[38:39]
	global_load_dwordx4 v[144:147], v100, s[40:41]
	global_load_dwordx4 v[148:151], v100, s[42:43]
	global_load_dwordx4 v[152:155], v101, s[36:37]
	global_load_dwordx4 v[156:159], v101, s[38:39]
	global_load_dwordx4 v[160:163], v101, s[40:41]
	global_load_dwordx4 v[164:167], v101, s[42:43]
	s_add_i32 s34, s25, s23
	s_mov_b32 s26, 0x3e38aa3b
	s_mov_b32 s27, 0x3e38aa3b
	s_sub_i32 s32, 0x400, s34
	s_ashr_i32 s32, s32, 4
	s_max_i32 s32, s32, 0
	s_min_i32 s32, s32, 6
	s_sub_i32 s33, 0x800, s34
	s_ashr_i32 s33, s33, 4
	s_max_i32 s33, s33, 0
	s_min_i32 s33, s33, 6
	s_cmp_le_u32 s33, 5
	s_cbranch_scc1 .Lepi_v5
	s_waitcnt vmcnt(0)
	s_cmp_lg_u32 s32, 6
	s_cbranch_scc1 .Lepi_r5
	v_pk_mul_f32 v[104:105], v[104:105], s[26:27]
	v_pk_mul_f32 v[106:107], v[106:107], s[26:27]
	v_pk_mul_f32 v[108:109], v[108:109], s[26:27]
	v_pk_mul_f32 v[110:111], v[110:111], s[26:27]
	v_pk_mul_f32 v[112:113], v[112:113], s[26:27]
	v_pk_mul_f32 v[114:115], v[114:115], s[26:27]
	v_pk_mul_f32 v[116:117], v[116:117], s[26:27]
	v_pk_mul_f32 v[118:119], v[118:119], s[26:27]
	v_pk_mul_f32 v[120:121], v[120:121], s[26:27]
	v_pk_mul_f32 v[122:123], v[122:123], s[26:27]
	v_pk_mul_f32 v[124:125], v[124:125], s[26:27]
	v_pk_mul_f32 v[126:127], v[126:127], s[26:27]
	v_pk_mul_f32 v[128:129], v[128:129], s[26:27]
	v_pk_mul_f32 v[130:131], v[130:131], s[26:27]
	v_pk_mul_f32 v[132:133], v[132:133], s[26:27]
	v_pk_mul_f32 v[134:135], v[134:135], s[26:27]
	v_pk_mul_f32 v[136:137], v[136:137], s[26:27]
	v_pk_mul_f32 v[138:139], v[138:139], s[26:27]
	v_pk_mul_f32 v[140:141], v[140:141], s[26:27]
	v_pk_mul_f32 v[142:143], v[142:143], s[26:27]
	v_pk_mul_f32 v[144:145], v[144:145], s[26:27]
	v_pk_mul_f32 v[146:147], v[146:147], s[26:27]
	v_pk_mul_f32 v[148:149], v[148:149], s[26:27]
	v_pk_mul_f32 v[150:151], v[150:151], s[26:27]
	v_pk_mul_f32 v[152:153], v[152:153], s[26:27]
	v_pk_mul_f32 v[154:155], v[154:155], s[26:27]
	v_pk_mul_f32 v[156:157], v[156:157], s[26:27]
	v_pk_mul_f32 v[158:159], v[158:159], s[26:27]
	v_pk_mul_f32 v[160:161], v[160:161], s[26:27]
	v_pk_mul_f32 v[162:163], v[162:163], s[26:27]
	v_pk_mul_f32 v[164:165], v[164:165], s[26:27]
	v_pk_mul_f32 v[166:167], v[166:167], s[26:27]
.Lepi_r5:
	v_pk_mul_f32 v[98:99], v[78:79], v[108:109] op_sel:[1,1] op_sel_hi:[1,0]
	v_pk_mul_f32 v[100:101], v[80:81], v[110:111] op_sel:[1,1] op_sel_hi:[1,0]
	v_pk_fma_f32 v[78:79], v[78:79], v[108:109], v[98:99] op_sel_hi:[0,1,1] neg_lo:[0,0,1]
	v_pk_fma_f32 v[80:81], v[80:81], v[110:111], v[100:101] op_sel_hi:[0,1,1] neg_lo:[0,0,1]
	v_cvt_pk_f16_f32 v78, v78, v79
	v_cvt_pk_f16_f32 v79, v80, v81
	ds_write_b64 v103, v[78:79] offset:160
	v_pk_mul_f32 v[98:99], v[62:63], v[124:125] op_sel:[1,1] op_sel_hi:[1,0]
	v_pk_mul_f32 v[100:101], v[64:65], v[126:127] op_sel:[1,1] op_sel_hi:[1,0]
	v_pk_fma_f32 v[62:63], v[62:63], v[124:125], v[98:99] op_sel_hi:[0,1,1] neg_lo:[0,0,1]
	v_pk_fma_f32 v[64:65], v[64:65], v[126:127], v[100:101] op_sel_hi:[0,1,1] neg_lo:[0,0,1]
	v_cvt_pk_f16_f32 v62, v62, v63
	v_cvt_pk_f16_f32 v63, v64, v65
	ds_write_b64 v103, v[62:63] offset:3488
	v_pk_mul_f32 v[98:99], v[34:35], v[140:141] op_sel:[1,1] op_sel_hi:[1,0]
	v_pk_mul_f32 v[100:101], v[36:37], v[142:143] op_sel:[1,1] op_sel_hi:[1,0]
	v_pk_fma_f32 v[34:35], v[34:35], v[140:141], v[98:99] op_sel_hi:[0,1,1] neg_lo:[0,0,1]
	v_pk_fma_f32 v[36:37], v[36:37], v[142:143], v[100:101] op_sel_hi:[0,1,1] neg_lo:[0,0,1]
	v_cvt_pk_f16_f32 v34, v34, v35
	v_cvt_pk_f16_f32 v35, v36, v37
	ds_write_b64 v103, v[34:35] offset:6816
	v_pk_mul_f32 v[98:99], v[2:3], v[156:157] op_sel:[1,1] op_sel_hi:[1,0]
	v_pk_mul_f32 v[100:101], v[4:5], v[158:159] op_sel:[1,1] op_sel_hi:[1,0]
	v_pk_fma_f32 v[2:3], v[2:3], v[156:157], v[98:99] op_sel_hi:[0,1,1] neg_lo:[0,0,1]
	v_pk_fma_f32 v[4:5], v[4:5], v[158:159], v[100:101] op_sel_hi:[0,1,1] neg_lo:[0,0,1]
	v_cvt_pk_f16_f32 v2, v2, v3
	v_cvt_pk_f16_f32 v3, v4, v5
	ds_write_b64 v103, v[2:3] offset:10144
	s_branch .Lepi_d5

.Lepi_d5:
	s_cmp_le_u32 s33, 4
	s_cbranch_scc1 .Lepi_v4
	s_waitcnt vmcnt(0)
	s_cmp_lg_u32 s32, 5
	s_cbranch_scc1 .Lepi_r4
	v_pk_mul_f32 v[104:105], v[104:105], s[26:27]
	v_pk_mul_f32 v[106:107], v[106:107], s[26:27]
	v_pk_mul_f32 v[108:109], v[108:109], s[26:27]
	v_pk_mul_f32 v[110:111], v[110:111], s[26:27]
	v_pk_mul_f32 v[112:113], v[112:113], s[26:27]
	v_pk_mul_f32 v[114:115], v[114:115], s[26:27]
	v_pk_mul_f32 v[116:117], v[116:117], s[26:27]
	v_pk_mul_f32 v[118:119], v[118:119], s[26:27]
	v_pk_mul_f32 v[120:121], v[120:121], s[26:27]
	v_pk_mul_f32 v[122:123], v[122:123], s[26:27]
	v_pk_mul_f32 v[124:125], v[124:125], s[26:27]
	v_pk_mul_f32 v[126:127], v[126:127], s[26:27]
	v_pk_mul_f32 v[128:129], v[128:129], s[26:27]
	v_pk_mul_f32 v[130:131], v[130:131], s[26:27]
	v_pk_mul_f32 v[132:133], v[132:133], s[26:27]
	v_pk_mul_f32 v[134:135], v[134:135], s[26:27]
	v_pk_mul_f32 v[136:137], v[136:137], s[26:27]
	v_pk_mul_f32 v[138:139], v[138:139], s[26:27]
	v_pk_mul_f32 v[140:141], v[140:141], s[26:27]
	v_pk_mul_f32 v[142:143], v[142:143], s[26:27]
	v_pk_mul_f32 v[144:145], v[144:145], s[26:27]
	v_pk_mul_f32 v[146:147], v[146:147], s[26:27]
	v_pk_mul_f32 v[148:149], v[148:149], s[26:27]
	v_pk_mul_f32 v[150:151], v[150:151], s[26:27]
	v_pk_mul_f32 v[152:153], v[152:153], s[26:27]
	v_pk_mul_f32 v[154:155], v[154:155], s[26:27]
	v_pk_mul_f32 v[156:157], v[156:157], s[26:27]
	v_pk_mul_f32 v[158:159], v[158:159], s[26:27]
	v_pk_mul_f32 v[160:161], v[160:161], s[26:27]
	v_pk_mul_f32 v[162:163], v[162:163], s[26:27]
	v_pk_mul_f32 v[164:165], v[164:165], s[26:27]
	v_pk_mul_f32 v[166:167], v[166:167], s[26:27]
.Lepi_r4:
	v_pk_mul_f32 v[98:99], v[82:83], v[104:105] op_sel:[1,1] op_sel_hi:[1,0]
	v_pk_mul_f32 v[100:101], v[84:85], v[106:107] op_sel:[1,1] op_sel_hi:[1,0]
	v_pk_fma_f32 v[82:83], v[82:83], v[104:105], v[98:99] op_sel_hi:[0,1,1] neg_lo:[0,0,1]
	v_pk_fma_f32 v[84:85], v[84:85], v[106:107], v[100:101] op_sel_hi:[0,1,1] neg_lo:[0,0,1]
	v_cvt_pk_f16_f32 v82, v82, v83
	v_cvt_pk_f16_f32 v83, v84, v85
	ds_write_b64 v103, v[82:83] offset:128
	v_pk_mul_f32 v[98:99], v[58:59], v[120:121] op_sel:[1,1] op_sel_hi:[1,0]
	v_pk_mul_f32 v[100:101], v[60:61], v[122:123] op_sel:[1,1] op_sel_hi:[1,0]
	v_pk_fma_f32 v[58:59], v[58:59], v[120:121], v[98:99] op_sel_hi:[0,1,1] neg_lo:[0,0,1]
	v_pk_fma_f32 v[60:61], v[60:61], v[122:123], v[100:101] op_sel_hi:[0,1,1] neg_lo:[0,0,1]
	v_cvt_pk_f16_f32 v58, v58, v59
	v_cvt_pk_f16_f32 v59, v60, v61
	ds_write_b64 v103, v[58:59] offset:3456
	v_pk_mul_f32 v[98:99], v[30:31], v[136:137] op_sel:[1,1] op_sel_hi:[1,0]
	v_pk_mul_f32 v[100:101], v[32:33], v[138:139] op_sel:[1,1] op_sel_hi:[1,0]
	v_pk_fma_f32 v[30:31], v[30:31], v[136:137], v[98:99] op_sel_hi:[0,1,1] neg_lo:[0,0,1]
	v_pk_fma_f32 v[32:33], v[32:33], v[138:139], v[100:101] op_sel_hi:[0,1,1] neg_lo:[0,0,1]
	v_cvt_pk_f16_f32 v30, v30, v31
	v_cvt_pk_f16_f32 v31, v32, v33
	ds_write_b64 v103, v[30:31] offset:6784
	v_pk_mul_f32 v[98:99], v[10:11], v[152:153] op_sel:[1,1] op_sel_hi:[1,0]
	v_pk_mul_f32 v[100:101], v[12:13], v[154:155] op_sel:[1,1] op_sel_hi:[1,0]
	v_pk_fma_f32 v[10:11], v[10:11], v[152:153], v[98:99] op_sel_hi:[0,1,1] neg_lo:[0,0,1]
	v_pk_fma_f32 v[12:13], v[12:13], v[154:155], v[100:101] op_sel_hi:[0,1,1] neg_lo:[0,0,1]
	v_cvt_pk_f16_f32 v10, v10, v11
	v_cvt_pk_f16_f32 v11, v12, v13
	ds_write_b64 v103, v[10:11] offset:10112
	s_branch .Lepi_d4

.Lepi_d4:
	s_cmp_le_u32 s33, 3
	s_cbranch_scc1 .Lepi_v3
	s_waitcnt vmcnt(0)
	s_cmp_lg_u32 s32, 4
	s_cbranch_scc1 .Lepi_r3
	v_pk_mul_f32 v[104:105], v[104:105], s[26:27]
	v_pk_mul_f32 v[106:107], v[106:107], s[26:27]
	v_pk_mul_f32 v[108:109], v[108:109], s[26:27]
	v_pk_mul_f32 v[110:111], v[110:111], s[26:27]
	v_pk_mul_f32 v[112:113], v[112:113], s[26:27]
	v_pk_mul_f32 v[114:115], v[114:115], s[26:27]
	v_pk_mul_f32 v[116:117], v[116:117], s[26:27]
	v_pk_mul_f32 v[118:119], v[118:119], s[26:27]
	v_pk_mul_f32 v[120:121], v[120:121], s[26:27]
	v_pk_mul_f32 v[122:123], v[122:123], s[26:27]
	v_pk_mul_f32 v[124:125], v[124:125], s[26:27]
	v_pk_mul_f32 v[126:127], v[126:127], s[26:27]
	v_pk_mul_f32 v[128:129], v[128:129], s[26:27]
	v_pk_mul_f32 v[130:131], v[130:131], s[26:27]
	v_pk_mul_f32 v[132:133], v[132:133], s[26:27]
	v_pk_mul_f32 v[134:135], v[134:135], s[26:27]
	v_pk_mul_f32 v[136:137], v[136:137], s[26:27]
	v_pk_mul_f32 v[138:139], v[138:139], s[26:27]
	v_pk_mul_f32 v[140:141], v[140:141], s[26:27]
	v_pk_mul_f32 v[142:143], v[142:143], s[26:27]
	v_pk_mul_f32 v[144:145], v[144:145], s[26:27]
	v_pk_mul_f32 v[146:147], v[146:147], s[26:27]
	v_pk_mul_f32 v[148:149], v[148:149], s[26:27]
	v_pk_mul_f32 v[150:151], v[150:151], s[26:27]
	v_pk_mul_f32 v[152:153], v[152:153], s[26:27]
	v_pk_mul_f32 v[154:155], v[154:155], s[26:27]
	v_pk_mul_f32 v[156:157], v[156:157], s[26:27]
	v_pk_mul_f32 v[158:159], v[158:159], s[26:27]
	v_pk_mul_f32 v[160:161], v[160:161], s[26:27]
	v_pk_mul_f32 v[162:163], v[162:163], s[26:27]
	v_pk_mul_f32 v[164:165], v[164:165], s[26:27]
	v_pk_mul_f32 v[166:167], v[166:167], s[26:27]
.Lepi_r3:
	v_pk_mul_f32 v[98:99], v[74:75], v[116:117] op_sel:[1,1] op_sel_hi:[1,0]
	v_pk_mul_f32 v[100:101], v[76:77], v[118:119] op_sel:[1,1] op_sel_hi:[1,0]
	v_pk_fma_f32 v[74:75], v[74:75], v[116:117], v[98:99] op_sel_hi:[0,1,1] neg_lo:[0,0,1]
	v_pk_fma_f32 v[76:77], v[76:77], v[118:119], v[100:101] op_sel_hi:[0,1,1] neg_lo:[0,0,1]
	v_cvt_pk_f16_f32 v74, v74, v75
	v_cvt_pk_f16_f32 v75, v76, v77
	ds_write_b64 v103, v[74:75] offset:96
	v_pk_mul_f32 v[98:99], v[50:51], v[132:133] op_sel:[1,1] op_sel_hi:[1,0]
	v_pk_mul_f32 v[100:101], v[52:53], v[134:135] op_sel:[1,1] op_sel_hi:[1,0]
	v_pk_fma_f32 v[50:51], v[50:51], v[132:133], v[98:99] op_sel_hi:[0,1,1] neg_lo:[0,0,1]
	v_pk_fma_f32 v[52:53], v[52:53], v[134:135], v[100:101] op_sel_hi:[0,1,1] neg_lo:[0,0,1]
	v_cvt_pk_f16_f32 v50, v50, v51
	v_cvt_pk_f16_f32 v51, v52, v53
	ds_write_b64 v103, v[50:51] offset:3424
	v_pk_mul_f32 v[98:99], v[38:39], v[148:149] op_sel:[1,1] op_sel_hi:[1,0]
	v_pk_mul_f32 v[100:101], v[40:41], v[150:151] op_sel:[1,1] op_sel_hi:[1,0]
	v_pk_fma_f32 v[38:39], v[38:39], v[148:149], v[98:99] op_sel_hi:[0,1,1] neg_lo:[0,0,1]
	v_pk_fma_f32 v[40:41], v[40:41], v[150:151], v[100:101] op_sel_hi:[0,1,1] neg_lo:[0,0,1]
	v_cvt_pk_f16_f32 v38, v38, v39
	v_cvt_pk_f16_f32 v39, v40, v41
	ds_write_b64 v103, v[38:39] offset:6752
	v_pk_mul_f32 v[98:99], v[14:15], v[164:165] op_sel:[1,1] op_sel_hi:[1,0]
	v_pk_mul_f32 v[100:101], v[16:17], v[166:167] op_sel:[1,1] op_sel_hi:[1,0]
	v_pk_fma_f32 v[14:15], v[14:15], v[164:165], v[98:99] op_sel_hi:[0,1,1] neg_lo:[0,0,1]
	v_pk_fma_f32 v[16:17], v[16:17], v[166:167], v[100:101] op_sel_hi:[0,1,1] neg_lo:[0,0,1]
	v_cvt_pk_f16_f32 v14, v14, v15
	v_cvt_pk_f16_f32 v15, v16, v17
	ds_write_b64 v103, v[14:15] offset:10080
	s_branch .Lepi_d3

.Lepi_d3:
	s_cmp_le_u32 s33, 2
	s_cbranch_scc1 .Lepi_v2
	s_waitcnt vmcnt(0)
	s_cmp_lg_u32 s32, 3
	s_cbranch_scc1 .Lepi_r2
	v_pk_mul_f32 v[104:105], v[104:105], s[26:27]
	v_pk_mul_f32 v[106:107], v[106:107], s[26:27]
	v_pk_mul_f32 v[108:109], v[108:109], s[26:27]
	v_pk_mul_f32 v[110:111], v[110:111], s[26:27]
	v_pk_mul_f32 v[112:113], v[112:113], s[26:27]
	v_pk_mul_f32 v[114:115], v[114:115], s[26:27]
	v_pk_mul_f32 v[116:117], v[116:117], s[26:27]
	v_pk_mul_f32 v[118:119], v[118:119], s[26:27]
	v_pk_mul_f32 v[120:121], v[120:121], s[26:27]
	v_pk_mul_f32 v[122:123], v[122:123], s[26:27]
	v_pk_mul_f32 v[124:125], v[124:125], s[26:27]
	v_pk_mul_f32 v[126:127], v[126:127], s[26:27]
	v_pk_mul_f32 v[128:129], v[128:129], s[26:27]
	v_pk_mul_f32 v[130:131], v[130:131], s[26:27]
	v_pk_mul_f32 v[132:133], v[132:133], s[26:27]
	v_pk_mul_f32 v[134:135], v[134:135], s[26:27]
	v_pk_mul_f32 v[136:137], v[136:137], s[26:27]
	v_pk_mul_f32 v[138:139], v[138:139], s[26:27]
	v_pk_mul_f32 v[140:141], v[140:141], s[26:27]
	v_pk_mul_f32 v[142:143], v[142:143], s[26:27]
	v_pk_mul_f32 v[144:145], v[144:145], s[26:27]
	v_pk_mul_f32 v[146:147], v[146:147], s[26:27]
	v_pk_mul_f32 v[148:149], v[148:149], s[26:27]
	v_pk_mul_f32 v[150:151], v[150:151], s[26:27]
	v_pk_mul_f32 v[152:153], v[152:153], s[26:27]
	v_pk_mul_f32 v[154:155], v[154:155], s[26:27]
	v_pk_mul_f32 v[156:157], v[156:157], s[26:27]
	v_pk_mul_f32 v[158:159], v[158:159], s[26:27]
	v_pk_mul_f32 v[160:161], v[160:161], s[26:27]
	v_pk_mul_f32 v[162:163], v[162:163], s[26:27]
	v_pk_mul_f32 v[164:165], v[164:165], s[26:27]
	v_pk_mul_f32 v[166:167], v[166:167], s[26:27]
.Lepi_r2:
	v_pk_mul_f32 v[98:99], v[86:87], v[112:113] op_sel:[1,1] op_sel_hi:[1,0]
	v_pk_mul_f32 v[100:101], v[88:89], v[114:115] op_sel:[1,1] op_sel_hi:[1,0]
	v_pk_fma_f32 v[86:87], v[86:87], v[112:113], v[98:99] op_sel_hi:[0,1,1] neg_lo:[0,0,1]
	v_pk_fma_f32 v[88:89], v[88:89], v[114:115], v[100:101] op_sel_hi:[0,1,1] neg_lo:[0,0,1]
	v_cvt_pk_f16_f32 v86, v86, v87
	v_cvt_pk_f16_f32 v87, v88, v89
	ds_write_b64 v103, v[86:87] offset:64
	v_pk_mul_f32 v[98:99], v[54:55], v[128:129] op_sel:[1,1] op_sel_hi:[1,0]
	v_pk_mul_f32 v[100:101], v[56:57], v[130:131] op_sel:[1,1] op_sel_hi:[1,0]
	v_pk_fma_f32 v[54:55], v[54:55], v[128:129], v[98:99] op_sel_hi:[0,1,1] neg_lo:[0,0,1]
	v_pk_fma_f32 v[56:57], v[56:57], v[130:131], v[100:101] op_sel_hi:[0,1,1] neg_lo:[0,0,1]
	v_cvt_pk_f16_f32 v54, v54, v55
	v_cvt_pk_f16_f32 v55, v56, v57
	ds_write_b64 v103, v[54:55] offset:3392
	v_pk_mul_f32 v[98:99], v[26:27], v[144:145] op_sel:[1,1] op_sel_hi:[1,0]
	v_pk_mul_f32 v[100:101], v[28:29], v[146:147] op_sel:[1,1] op_sel_hi:[1,0]
	v_pk_fma_f32 v[26:27], v[26:27], v[144:145], v[98:99] op_sel_hi:[0,1,1] neg_lo:[0,0,1]
	v_pk_fma_f32 v[28:29], v[28:29], v[146:147], v[100:101] op_sel_hi:[0,1,1] neg_lo:[0,0,1]
	v_cvt_pk_f16_f32 v26, v26, v27
	v_cvt_pk_f16_f32 v27, v28, v29
	ds_write_b64 v103, v[26:27] offset:6720
	v_pk_mul_f32 v[98:99], v[6:7], v[160:161] op_sel:[1,1] op_sel_hi:[1,0]
	v_pk_mul_f32 v[100:101], v[8:9], v[162:163] op_sel:[1,1] op_sel_hi:[1,0]
	v_pk_fma_f32 v[6:7], v[6:7], v[160:161], v[98:99] op_sel_hi:[0,1,1] neg_lo:[0,0,1]
	v_pk_fma_f32 v[8:9], v[8:9], v[162:163], v[100:101] op_sel_hi:[0,1,1] neg_lo:[0,0,1]
	v_cvt_pk_f16_f32 v6, v6, v7
	v_cvt_pk_f16_f32 v7, v8, v9
	ds_write_b64 v103, v[6:7] offset:10048
	s_branch .Lepi_d2

.Lepi_d2:
	s_cmp_le_u32 s33, 1
	s_cbranch_scc1 .Lepi_v1
	s_waitcnt vmcnt(0)
	s_cmp_lg_u32 s32, 2
	s_cbranch_scc1 .Lepi_r1
	v_pk_mul_f32 v[104:105], v[104:105], s[26:27]
	v_pk_mul_f32 v[106:107], v[106:107], s[26:27]
	v_pk_mul_f32 v[108:109], v[108:109], s[26:27]
	v_pk_mul_f32 v[110:111], v[110:111], s[26:27]
	v_pk_mul_f32 v[112:113], v[112:113], s[26:27]
	v_pk_mul_f32 v[114:115], v[114:115], s[26:27]
	v_pk_mul_f32 v[116:117], v[116:117], s[26:27]
	v_pk_mul_f32 v[118:119], v[118:119], s[26:27]
	v_pk_mul_f32 v[120:121], v[120:121], s[26:27]
	v_pk_mul_f32 v[122:123], v[122:123], s[26:27]
	v_pk_mul_f32 v[124:125], v[124:125], s[26:27]
	v_pk_mul_f32 v[126:127], v[126:127], s[26:27]
	v_pk_mul_f32 v[128:129], v[128:129], s[26:27]
	v_pk_mul_f32 v[130:131], v[130:131], s[26:27]
	v_pk_mul_f32 v[132:133], v[132:133], s[26:27]
	v_pk_mul_f32 v[134:135], v[134:135], s[26:27]
	v_pk_mul_f32 v[136:137], v[136:137], s[26:27]
	v_pk_mul_f32 v[138:139], v[138:139], s[26:27]
	v_pk_mul_f32 v[140:141], v[140:141], s[26:27]
	v_pk_mul_f32 v[142:143], v[142:143], s[26:27]
	v_pk_mul_f32 v[144:145], v[144:145], s[26:27]
	v_pk_mul_f32 v[146:147], v[146:147], s[26:27]
	v_pk_mul_f32 v[148:149], v[148:149], s[26:27]
	v_pk_mul_f32 v[150:151], v[150:151], s[26:27]
	v_pk_mul_f32 v[152:153], v[152:153], s[26:27]
	v_pk_mul_f32 v[154:155], v[154:155], s[26:27]
	v_pk_mul_f32 v[156:157], v[156:157], s[26:27]
	v_pk_mul_f32 v[158:159], v[158:159], s[26:27]
	v_pk_mul_f32 v[160:161], v[160:161], s[26:27]
	v_pk_mul_f32 v[162:163], v[162:163], s[26:27]
	v_pk_mul_f32 v[164:165], v[164:165], s[26:27]
	v_pk_mul_f32 v[166:167], v[166:167], s[26:27]
.Lepi_r1:
	v_pk_mul_f32 v[98:99], v[90:91], v[108:109] op_sel:[1,1] op_sel_hi:[1,0]
	v_pk_mul_f32 v[100:101], v[92:93], v[110:111] op_sel:[1,1] op_sel_hi:[1,0]
	v_pk_fma_f32 v[90:91], v[90:91], v[108:109], v[98:99] op_sel_hi:[0,1,1] neg_lo:[0,0,1]
	v_pk_fma_f32 v[92:93], v[92:93], v[110:111], v[100:101] op_sel_hi:[0,1,1] neg_lo:[0,0,1]
	v_cvt_pk_f16_f32 v90, v90, v91
	v_cvt_pk_f16_f32 v91, v92, v93
	ds_write_b64 v103, v[90:91] offset:32
	v_pk_mul_f32 v[98:99], v[66:67], v[124:125] op_sel:[1,1] op_sel_hi:[1,0]
	v_pk_mul_f32 v[100:101], v[68:69], v[126:127] op_sel:[1,1] op_sel_hi:[1,0]
	v_pk_fma_f32 v[66:67], v[66:67], v[124:125], v[98:99] op_sel_hi:[0,1,1] neg_lo:[0,0,1]
	v_pk_fma_f32 v[68:69], v[68:69], v[126:127], v[100:101] op_sel_hi:[0,1,1] neg_lo:[0,0,1]
	v_cvt_pk_f16_f32 v66, v66, v67
	v_cvt_pk_f16_f32 v67, v68, v69
	ds_write_b64 v103, v[66:67] offset:3360
	v_pk_mul_f32 v[98:99], v[42:43], v[140:141] op_sel:[1,1] op_sel_hi:[1,0]
	v_pk_mul_f32 v[100:101], v[44:45], v[142:143] op_sel:[1,1] op_sel_hi:[1,0]
	v_pk_fma_f32 v[42:43], v[42:43], v[140:141], v[98:99] op_sel_hi:[0,1,1] neg_lo:[0,0,1]
	v_pk_fma_f32 v[44:45], v[44:45], v[142:143], v[100:101] op_sel_hi:[0,1,1] neg_lo:[0,0,1]
	v_cvt_pk_f16_f32 v42, v42, v43
	v_cvt_pk_f16_f32 v43, v44, v45
	ds_write_b64 v103, v[42:43] offset:6688
	v_pk_mul_f32 v[98:99], v[18:19], v[156:157] op_sel:[1,1] op_sel_hi:[1,0]
	v_pk_mul_f32 v[100:101], v[20:21], v[158:159] op_sel:[1,1] op_sel_hi:[1,0]
	v_pk_fma_f32 v[18:19], v[18:19], v[156:157], v[98:99] op_sel_hi:[0,1,1] neg_lo:[0,0,1]
	v_pk_fma_f32 v[20:21], v[20:21], v[158:159], v[100:101] op_sel_hi:[0,1,1] neg_lo:[0,0,1]
	v_cvt_pk_f16_f32 v18, v18, v19
	v_cvt_pk_f16_f32 v19, v20, v21
	ds_write_b64 v103, v[18:19] offset:10016
	s_branch .Lepi_d1

.Lepi_d1:
	s_cmp_le_u32 s33, 0
	s_cbranch_scc1 .Lepi_v0
	s_waitcnt vmcnt(0)
	s_cmp_lg_u32 s32, 1
	s_cbranch_scc1 .Lepi_r0
	v_pk_mul_f32 v[104:105], v[104:105], s[26:27]
	v_pk_mul_f32 v[106:107], v[106:107], s[26:27]
	v_pk_mul_f32 v[108:109], v[108:109], s[26:27]
	v_pk_mul_f32 v[110:111], v[110:111], s[26:27]
	v_pk_mul_f32 v[112:113], v[112:113], s[26:27]
	v_pk_mul_f32 v[114:115], v[114:115], s[26:27]
	v_pk_mul_f32 v[116:117], v[116:117], s[26:27]
	v_pk_mul_f32 v[118:119], v[118:119], s[26:27]
	v_pk_mul_f32 v[120:121], v[120:121], s[26:27]
	v_pk_mul_f32 v[122:123], v[122:123], s[26:27]
	v_pk_mul_f32 v[124:125], v[124:125], s[26:27]
	v_pk_mul_f32 v[126:127], v[126:127], s[26:27]
	v_pk_mul_f32 v[128:129], v[128:129], s[26:27]
	v_pk_mul_f32 v[130:131], v[130:131], s[26:27]
	v_pk_mul_f32 v[132:133], v[132:133], s[26:27]
	v_pk_mul_f32 v[134:135], v[134:135], s[26:27]
	v_pk_mul_f32 v[136:137], v[136:137], s[26:27]
	v_pk_mul_f32 v[138:139], v[138:139], s[26:27]
	v_pk_mul_f32 v[140:141], v[140:141], s[26:27]
	v_pk_mul_f32 v[142:143], v[142:143], s[26:27]
	v_pk_mul_f32 v[144:145], v[144:145], s[26:27]
	v_pk_mul_f32 v[146:147], v[146:147], s[26:27]
	v_pk_mul_f32 v[148:149], v[148:149], s[26:27]
	v_pk_mul_f32 v[150:151], v[150:151], s[26:27]
	v_pk_mul_f32 v[152:153], v[152:153], s[26:27]
	v_pk_mul_f32 v[154:155], v[154:155], s[26:27]
	v_pk_mul_f32 v[156:157], v[156:157], s[26:27]
	v_pk_mul_f32 v[158:159], v[158:159], s[26:27]
	v_pk_mul_f32 v[160:161], v[160:161], s[26:27]
	v_pk_mul_f32 v[162:163], v[162:163], s[26:27]
	v_pk_mul_f32 v[164:165], v[164:165], s[26:27]
	v_pk_mul_f32 v[166:167], v[166:167], s[26:27]
.Lepi_r0:
	v_pk_mul_f32 v[98:99], v[94:95], v[104:105] op_sel:[1,1] op_sel_hi:[1,0]
	v_pk_mul_f32 v[100:101], v[96:97], v[106:107] op_sel:[1,1] op_sel_hi:[1,0]
	v_pk_fma_f32 v[94:95], v[94:95], v[104:105], v[98:99] op_sel_hi:[0,1,1] neg_lo:[0,0,1]
	v_pk_fma_f32 v[96:97], v[96:97], v[106:107], v[100:101] op_sel_hi:[0,1,1] neg_lo:[0,0,1]
	v_cvt_pk_f16_f32 v94, v94, v95
	v_cvt_pk_f16_f32 v95, v96, v97
	ds_write_b64 v103, v[94:95] offset:0
	v_pk_mul_f32 v[98:99], v[70:71], v[120:121] op_sel:[1,1] op_sel_hi:[1,0]
	v_pk_mul_f32 v[100:101], v[72:73], v[122:123] op_sel:[1,1] op_sel_hi:[1,0]
	v_pk_fma_f32 v[70:71], v[70:71], v[120:121], v[98:99] op_sel_hi:[0,1,1] neg_lo:[0,0,1]
	v_pk_fma_f32 v[72:73], v[72:73], v[122:123], v[100:101] op_sel_hi:[0,1,1] neg_lo:[0,0,1]
	v_cvt_pk_f16_f32 v70, v70, v71
	v_cvt_pk_f16_f32 v71, v72, v73
	ds_write_b64 v103, v[70:71] offset:3328
	v_pk_mul_f32 v[98:99], v[46:47], v[136:137] op_sel:[1,1] op_sel_hi:[1,0]
	v_pk_mul_f32 v[100:101], v[48:49], v[138:139] op_sel:[1,1] op_sel_hi:[1,0]
	v_pk_fma_f32 v[46:47], v[46:47], v[136:137], v[98:99] op_sel_hi:[0,1,1] neg_lo:[0,0,1]
	v_pk_fma_f32 v[48:49], v[48:49], v[138:139], v[100:101] op_sel_hi:[0,1,1] neg_lo:[0,0,1]
	v_cvt_pk_f16_f32 v46, v46, v47
	v_cvt_pk_f16_f32 v47, v48, v49
	ds_write_b64 v103, v[46:47] offset:6656
	v_pk_mul_f32 v[98:99], v[22:23], v[152:153] op_sel:[1,1] op_sel_hi:[1,0]
	v_pk_mul_f32 v[100:101], v[24:25], v[154:155] op_sel:[1,1] op_sel_hi:[1,0]
	v_pk_fma_f32 v[22:23], v[22:23], v[152:153], v[98:99] op_sel_hi:[0,1,1] neg_lo:[0,0,1]
	v_pk_fma_f32 v[24:25], v[24:25], v[154:155], v[100:101] op_sel_hi:[0,1,1] neg_lo:[0,0,1]
	v_cvt_pk_f16_f32 v22, v22, v23
	v_cvt_pk_f16_f32 v23, v24, v25
	ds_write_b64 v103, v[22:23] offset:9984
	s_branch .Lepi_d0
